# P0 expert items: permute item id so a workgroup's 8 waves convert 8 consecutive k-blocks of one column strip (each fp8 dst row's 2KB written by 2 neighbouring WGs on one XCD)
# baseline (speedup 1.0000x reference)
; __device__ __forceinline__ MoeItem moe_item(const float* wg, const float* wu, const float* wd, const float* win, const float* wout, const float* wpn, const float* wpd, unsigned char* ws, int r, int lane) {
;     ...
;     const int mat = r / MOE_IE, q = r % MOE_IE, e = mat / 3, which = mat % 3, kb = q / 64, nb = q % 64, n0 = nb * 32;
;     const float* src = (which == 0 ? wg : (which == 1 ? wu : wd)) + (size_t)e * DM * DFF + (size_t)(kb * 128 + (lane >> 5)) * DFF + n0 + (lane & 31);
;     unsigned char* dst;
;     if (which < 2) dst = ws + WS_WGUT + ((size_t)(e * 16 + (n0 >> 7)) * 256 + which * 128 + (n0 & 127)) * DM;
;     else dst = ws + WS_WDT + ((size_t)e * DM + n0) * DFF;
;     MoeItem it; it.stride = DFF; it.dpitch = DM; it.src = src; it.dst = dst + kb * 128 + (size_t)(lane >> 3) * DM + 16 * (lane & 7); return it;
;     ...
;         const int nmine = (NMOE - gw + NGW - 1) / NGW;
;         const int last = gw + (nmine - 1) * NGW;
;         MoeItem ia = moe_item(wg, wu, wd, win, wout, wpn, wpd, F.ws, gw, F.lane), ib = ia;
.LBB0_49:
	s_abs_i32 s6, s72
	v_cvt_f32_u32_e32 v1, s6
	s_sub_i32 s4, s72, s3
	s_add_i32 s68, s4, 0x193ff
	s_sub_i32 s4, 0xfffe6c01, s4
	v_rcp_iflag_f32_e32 v1, v1
	s_max_i32 s7, s68, s4
	s_sub_i32 s4, 0, s6
	v_mul_f32_e32 v1, 0x4f7ffffe, v1
	v_cvt_u32_f32_e32 v1, v1
	s_nop 0
	v_readfirstlane_b32 s5, v1
	s_mul_i32 s4, s4, s5
	s_mul_hi_u32 s4, s5, s4
	s_add_i32 s5, s5, s4
	s_cmp_lt_i32 s3, 0x19000
	s_mul_hi_u32 s47, s7, s5
	s_cbranch_scc0 .LBB0_54
	s_cmp_lt_i32 s3, 0x18c00
	s_cbranch_scc0 .LBB0_56
	s_cmp_lt_i32 s3, 0x18000
	s_cbranch_scc0 .LBB0_57
	s_and_b32 s4, s3, 15
	s_lshl_b32 s4, s4, 6
	s_bfe_u32 s5, s3, 0x60004
	s_and_b32 s99, s3, 0xfffffc00
	s_or_b32 s99, s99, s4
	s_or_b32 s99, s99, s5
	s_ashr_i32 s4, s99, 31
	s_lshr_b32 s4, s4, 22
	s_add_i32 s4, s99, s4
	s_ashr_i32 s5, s4, 10
	s_and_b32 s4, s4, 0xfc00
	s_sub_i32 s38, s99, s4
	s_mul_hi_i32 s4, s99, 0x2aaaaaab
	s_lshr_b32 s39, s4, 31
	s_ashr_i32 s4, s4, 9
	s_add_i32 s4, s4, s39
	s_mul_hi_i32 s39, s5, 0x55555556
	s_lshr_b32 s42, s39, 31
	s_add_i32 s39, s39, s42
	s_mul_i32 s39, s39, 3
	s_sub_i32 s69, s5, s39
	s_sext_i32_i16 s5, s38
	s_bfe_u32 s5, s5, 0x60019
	s_add_i32 s42, s38, s5
	s_and_b32 s5, s42, 0xffc0
	s_sub_i32 s5, s38, s5
	s_sext_i32_i16 s70, s5
	s_lshl_b32 s38, s70, 5
	s_ashr_i32 s5, s4, 31
	s_ashr_i32 s39, s38, 31
	s_cmp_gt_i32 s69, 1
	s_sext_i32_i16 s71, s42
	s_cbranch_scc0 .LBB0_58
	s_lshl_b64 s[42:43], s[4:5], 22
	s_lshl_b64 s[44:45], s[38:39], 11
	s_add_u32 s42, s82, s42
	s_addc_u32 s43, s83, s43
	s_add_u32 s42, s42, s44
	s_addc_u32 s43, s43, s45
	s_add_u32 s42, s42, 0x24000000
	s_addc_u32 s43, s43, 0
	s_mov_b64 s[44:45], 0
	s_branch .LBB0_59

; #define MOE_LOAD(v, it) do { _Pragma("unroll") for (int i_ = 0; i_ < 64; ++i_) v[i_] = __builtin_nontemporal_load((it).src + (size_t)(2 * i_) * (it).stride); } while (0)
; __device__ __forceinline__ MoeItem moe_item(const float* wg, const float* wu, const float* wd, const float* win, const float* wout, const float* wpn, const float* wpd, unsigned char* ws, int r, int lane) {
;     ...
;     const int mat = r / MOE_IE, q = r % MOE_IE, e = mat / 3, which = mat % 3, kb = q / 64, nb = q % 64, n0 = nb * 32;
;     const float* src = (which == 0 ? wg : (which == 1 ? wu : wd)) + (size_t)e * DM * DFF + (size_t)(kb * 128 + (lane >> 5)) * DFF + n0 + (lane & 31);
;     unsigned char* dst;
;     if (which < 2) dst = ws + WS_WGUT + ((size_t)(e * 16 + (n0 >> 7)) * 256 + which * 128 + (n0 & 127)) * DM;
;     else dst = ws + WS_WDT + ((size_t)e * DM + n0) * DFF;
;     MoeItem it; it.stride = DFF; it.dpitch = DM; it.src = src; it.dst = dst + kb * 128 + (size_t)(lane >> 3) * DM + 16 * (lane & 7); return it;
;     ...
;             const int it1 = gw + (j + 1) * NGW, it2 = gw + (j + 2) * NGW;
;             ib = moe_item(wg, wu, wd, win, wout, wpn, wpd, F.ws, it1 <= last ? it1 : last, F.lane); MOE_LOAD(vb, ib);
.LBB0_81:
	s_add_i32 s4, s72, s3
	s_min_i32 s70, s4, s7
	s_cmp_lt_i32 s70, 0x19000
	s_mov_b64 s[42:43], -1
	s_cbranch_scc0 .LBB0_102
	s_cmp_lt_i32 s70, 0x18c00
	s_cbranch_scc0 .LBB0_99
	s_cmp_lt_i32 s70, 0x18000
	s_cbranch_scc0 .LBB0_89
	s_and_b32 s4, s70, 15
	s_lshl_b32 s4, s4, 6
	s_bfe_u32 s44, s70, 0x60004
	s_and_b32 s70, s70, 0xfffffc00
	s_or_b32 s70, s70, s4
	s_or_b32 s70, s70, s44
	s_ashr_i32 s4, s70, 31
	s_lshr_b32 s4, s4, 22
	s_add_i32 s4, s70, s4
	s_ashr_i32 s43, s4, 10
	s_and_b32 s4, s4, 0xfc00
	s_sub_i32 s44, s70, s4
	s_mul_hi_i32 s4, s70, 0x2aaaaaab
	s_lshr_b32 s42, s4, 31
	s_ashr_i32 s4, s4, 9
	s_add_i32 s42, s4, s42
	s_mul_hi_i32 s4, s43, 0x55555556
	s_lshr_b32 s45, s4, 31
	s_add_i32 s4, s4, s45
	s_mul_i32 s4, s4, 3
	s_sub_i32 s4, s43, s4
	s_sext_i32_i16 s43, s44
	s_bfe_u32 s43, s43, 0x60019
	s_add_i32 s71, s44, s43
	s_and_b32 s43, s71, 0xffc0
	s_sub_i32 s43, s44, s43
	s_sext_i32_i16 s84, s43
	s_lshl_b32 s44, s84, 5
	s_ashr_i32 s43, s42, 31
	s_ashr_i32 s45, s44, 31
	s_cmp_gt_i32 s4, 1
	s_mov_b64 s[68:69], -1
	s_cbranch_scc0 .LBB0_86
	s_lshl_b64 s[46:47], s[42:43], 22
	s_lshl_b64 s[68:69], s[44:45], 11
	s_add_u32 s46, s73, s46
	s_addc_u32 s47, s74, s47
	s_add_u32 s46, s46, s68
	s_addc_u32 s47, s47, s69
	s_mov_b64 s[68:69], 0

; #define MOE_LOAD(v, it) do { _Pragma("unroll") for (int i_ = 0; i_ < 64; ++i_) v[i_] = __builtin_nontemporal_load((it).src + (size_t)(2 * i_) * (it).stride); } while (0)
;     ...
;             ib = moe_item(wg, wu, wd, win, wout, wpn, wpd, F.ws, it1 <= last ? it1 : last, F.lane); MOE_LOAD(vb, ib);
;             MOE_PROC(va, ia);
.LBB0_105:
	s_lshl_b64 s[46:47], s[46:47], 3
	global_load_dword v93, v[16:17], off nt
	v_lshl_add_u64 v[16:17], v[16:17], 0, s[46:47]
	v_lshl_add_u64 v[94:95], v[16:17], 0, s[46:47]
	v_lshl_add_u64 v[96:97], v[94:95], 0, s[46:47]
	v_lshl_add_u64 v[102:103], v[96:97], 0, s[46:47]
	v_lshl_add_u64 v[104:105], v[102:103], 0, s[46:47]
	v_lshl_add_u64 v[106:107], v[104:105], 0, s[46:47]
	v_lshl_add_u64 v[108:109], v[106:107], 0, s[46:47]
	v_lshl_add_u64 v[110:111], v[108:109], 0, s[46:47]
	global_load_dword v101, v[16:17], off nt
	global_load_dword v99, v[94:95], off nt
	global_load_dword v100, v[96:97], off nt
	s_nop 0
	global_load_dword v97, v[102:103], off nt
	global_load_dword v98, v[104:105], off nt
	global_load_dword v95, v[106:107], off nt
	global_load_dword v96, v[108:109], off nt
	global_load_dword v94, v[110:111], off nt
	v_lshl_add_u64 v[16:17], v[110:111], 0, s[46:47]
	s_waitcnt vmcnt(9)
	ds_write2st64_b32 v28, v87, v92 offset1:1
	v_lshl_add_u64 v[102:103], v[16:17], 0, s[46:47]
	global_load_dword v124, v[16:17], off nt
	global_load_dword v104, v[102:103], off nt
	v_lshl_add_u64 v[16:17], v[102:103], 0, s[46:47]
	global_load_dword v114, v[16:17], off nt
	v_lshl_add_u64 v[16:17], v[16:17], 0, s[46:47]
	global_load_dword v105, v[16:17], off nt
	v_lshl_add_u64 v[16:17], v[16:17], 0, s[46:47]
	global_load_dword v115, v[16:17], off nt
	v_lshl_add_u64 v[16:17], v[16:17], 0, s[46:47]
	global_load_dword v106, v[16:17], off nt
	v_lshl_add_u64 v[16:17], v[16:17], 0, s[46:47]
	global_load_dword v116, v[16:17], off nt
	v_lshl_add_u64 v[16:17], v[16:17], 0, s[46:47]
	global_load_dword v107, v[16:17], off nt
	v_lshl_add_u64 v[16:17], v[16:17], 0, s[46:47]
	global_load_dword v117, v[16:17], off nt
	v_lshl_add_u64 v[16:17], v[16:17], 0, s[46:47]
	global_load_dword v108, v[16:17], off nt
	v_lshl_add_u64 v[16:17], v[16:17], 0, s[46:47]
	global_load_dword v118, v[16:17], off nt
	v_lshl_add_u64 v[16:17], v[16:17], 0, s[46:47]
	global_load_dword v109, v[16:17], off nt
	v_lshl_add_u64 v[16:17], v[16:17], 0, s[46:47]
	global_load_dword v119, v[16:17], off nt
	v_lshl_add_u64 v[16:17], v[16:17], 0, s[46:47]
	global_load_dword v110, v[16:17], off nt
	v_lshl_add_u64 v[16:17], v[16:17], 0, s[46:47]
	global_load_dword v120, v[16:17], off nt
	v_lshl_add_u64 v[16:17], v[16:17], 0, s[46:47]
	global_load_dword v111, v[16:17], off nt
	v_lshl_add_u64 v[16:17], v[16:17], 0, s[46:47]
	global_load_dword v121, v[16:17], off nt
	v_lshl_add_u64 v[16:17], v[16:17], 0, s[46:47]
	global_load_dword v112, v[16:17], off nt
	v_lshl_add_u64 v[16:17], v[16:17], 0, s[46:47]
	global_load_dword v122, v[16:17], off nt
	v_lshl_add_u64 v[16:17], v[16:17], 0, s[46:47]
	global_load_dword v102, v[16:17], off nt
	v_lshl_add_u64 v[16:17], v[16:17], 0, s[46:47]
	global_load_dword v103, v[16:17], off nt
	v_lshl_add_u64 v[16:17], v[16:17], 0, s[46:47]
	global_load_dword v113, v[16:17], off nt
	v_lshl_add_u64 v[16:17], v[16:17], 0, s[46:47]
	global_load_dword v123, v[16:17], off nt
	v_lshl_add_u64 v[16:17], v[16:17], 0, s[46:47]
	global_load_dword v125, v[16:17], off nt
	v_lshl_add_u64 v[16:17], v[16:17], 0, s[46:47]
	global_load_dword v126, v[16:17], off nt
	v_lshl_add_u64 v[16:17], v[16:17], 0, s[46:47]
	global_load_dword v127, v[16:17], off nt
	v_lshl_add_u64 v[16:17], v[16:17], 0, s[46:47]
	global_load_dword v128, v[16:17], off nt
	v_lshl_add_u64 v[16:17], v[16:17], 0, s[46:47]
	global_load_dword v129, v[16:17], off nt
	v_lshl_add_u64 v[16:17], v[16:17], 0, s[46:47]
	global_load_dword v130, v[16:17], off nt
	v_lshl_add_u64 v[16:17], v[16:17], 0, s[46:47]
	global_load_dword v131, v[16:17], off nt
	v_lshl_add_u64 v[16:17], v[16:17], 0, s[46:47]
	global_load_dword v132, v[16:17], off nt
	v_lshl_add_u64 v[16:17], v[16:17], 0, s[46:47]
	global_load_dword v133, v[16:17], off nt
	v_lshl_add_u64 v[16:17], v[16:17], 0, s[46:47]
	global_load_dword v134, v[16:17], off nt
	v_lshl_add_u64 v[16:17], v[16:17], 0, s[46:47]
	global_load_dword v135, v[16:17], off nt
	v_lshl_add_u64 v[16:17], v[16:17], 0, s[46:47]
	global_load_dword v136, v[16:17], off nt
	v_lshl_add_u64 v[16:17], v[16:17], 0, s[46:47]
	global_load_dword v137, v[16:17], off nt
	v_lshl_add_u64 v[16:17], v[16:17], 0, s[46:47]
	global_load_dword v138, v[16:17], off nt
	v_lshl_add_u64 v[16:17], v[16:17], 0, s[46:47]
	global_load_dword v139, v[16:17], off nt
	v_lshl_add_u64 v[16:17], v[16:17], 0, s[46:47]
	global_load_dword v140, v[16:17], off nt
	v_lshl_add_u64 v[16:17], v[16:17], 0, s[46:47]
	global_load_dword v141, v[16:17], off nt
	v_lshl_add_u64 v[16:17], v[16:17], 0, s[46:47]
	global_load_dword v142, v[16:17], off nt
	v_lshl_add_u64 v[16:17], v[16:17], 0, s[46:47]
	global_load_dword v143, v[16:17], off nt
	v_lshl_add_u64 v[16:17], v[16:17], 0, s[46:47]
	global_load_dword v144, v[16:17], off nt
	v_lshl_add_u64 v[16:17], v[16:17], 0, s[46:47]
	global_load_dword v146, v[16:17], off nt
	v_lshl_add_u64 v[16:17], v[16:17], 0, s[46:47]
	global_load_dword v147, v[16:17], off nt
	v_lshl_add_u64 v[16:17], v[16:17], 0, s[46:47]
	global_load_dword v148, v[16:17], off nt
	v_lshl_add_u64 v[16:17], v[16:17], 0, s[46:47]
	global_load_dword v149, v[16:17], off nt
	v_lshl_add_u64 v[16:17], v[16:17], 0, s[46:47]
	global_load_dword v151, v[16:17], off nt
	v_lshl_add_u64 v[16:17], v[16:17], 0, s[46:47]
	global_load_dword v152, v[16:17], off nt
	v_lshl_add_u64 v[16:17], v[16:17], 0, s[46:47]
	global_load_dword v153, v[16:17], off nt
	v_lshl_add_u64 v[16:17], v[16:17], 0, s[46:47]
	global_load_dword v154, v[16:17], off nt
	v_lshl_add_u64 v[16:17], v[16:17], 0, s[46:47]
	global_load_dword v155, v[16:17], off nt
	v_lshl_add_u64 v[16:17], v[16:17], 0, s[46:47]
	global_load_dword v157, v[16:17], off nt
	v_lshl_add_u64 v[16:17], v[16:17], 0, s[46:47]
	global_load_dword v158, v[16:17], off nt
	v_lshl_add_u64 v[16:17], v[16:17], 0, s[46:47]
	ds_write2st64_b32 v28, v91, v90 offset0:2 offset1:3
	ds_write2st64_b32 v28, v89, v88 offset0:4 offset1:5
	ds_write2st64_b32 v28, v86, v85 offset0:6 offset1:7
	ds_write2st64_b32 v21, v83, v84 offset0:8 offset1:9
	ds_write2st64_b32 v21, v79, v80 offset0:10 offset1:11
	ds_write2st64_b32 v21, v75, v76 offset0:12 offset1:13
	ds_write2st64_b32 v21, v71, v72 offset0:14 offset1:15
	ds_write2st64_b32 v22, v65, v66 offset0:16 offset1:17
	ds_write2st64_b32 v22, v61, v62 offset0:18 offset1:19
	ds_write2st64_b32 v22, v57, v58 offset0:20 offset1:21
	ds_write2st64_b32 v22, v53, v54 offset0:22 offset1:23
	ds_write2st64_b32 v23, v45, v46 offset0:24 offset1:25
	ds_write2st64_b32 v23, v35, v36 offset0:26 offset1:27
	ds_write2st64_b32 v23, v33, v34 offset0:28 offset1:29
	ds_write2st64_b32 v23, v31, v32 offset0:30 offset1:31
	ds_write2st64_b32 v24, v29, v30 offset0:32 offset1:33
	ds_write2st64_b32 v24, v81, v82 offset0:34 offset1:35
	ds_write2st64_b32 v24, v77, v78 offset0:36 offset1:37
	ds_write2st64_b32 v24, v73, v74 offset0:38 offset1:39
	ds_write2st64_b32 v25, v69, v70 offset0:40 offset1:41
	ds_write2st64_b32 v25, v67, v68 offset0:42 offset1:43
	ds_write2st64_b32 v25, v63, v64 offset0:44 offset1:45
	ds_write2st64_b32 v25, v59, v60 offset0:46 offset1:47
	ds_write2st64_b32 v26, v55, v56 offset0:48 offset1:49
	ds_write2st64_b32 v26, v51, v52 offset0:50 offset1:51
	global_load_dword v159, v[16:17], off nt
	ds_write2st64_b32 v26, v38, v39 offset0:52 offset1:53
	ds_write2st64_b32 v26, v40, v42 offset0:54 offset1:55
	ds_write2st64_b32 v27, v37, v41 offset0:56 offset1:57
	ds_write2st64_b32 v27, v43, v44 offset0:58 offset1:59
	ds_write2st64_b32 v27, v47, v48 offset0:60 offset1:61
	ds_write2st64_b32 v27, v49, v50 offset0:62 offset1:63
	s_waitcnt lgkmcnt(0)
	ds_read2_b32 v[16:17], v1 offset1:32
	v_mov_b32_e32 v30, 0
	ds_read2_b32 v[32:33], v1 offset0:128 offset1:160
	v_mov_b32_e32 v31, 0
	v_add_u32_e32 v145, 0x400, v1
	s_waitcnt lgkmcnt(1)
	v_mul_f32_e32 v4, 0x42800000, v16
	v_mul_f32_e32 v15, 0x42800000, v17
	ds_read2_b32 v[16:17], v1 offset0:64 offset1:96
	v_cvt_pk_fp8_f32 v30, v4, v15
	ds_read2_b32 v[34:35], v145 offset0:128 offset1:160
	v_add_u32_e32 v150, 0x400, v9
	ds_read2_b32 v[38:39], v150 offset0:128 offset1:160
	s_waitcnt lgkmcnt(2)
	v_mul_f32_e32 v4, 0x42800000, v16
	v_mul_f32_e32 v15, 0x42800000, v17
	ds_read2_b32 v[16:17], v1 offset0:192 offset1:224
	v_cvt_pk_fp8_f32 v30, v4, v15 op_sel:[0,0,1]
	v_mul_f32_e32 v4, 0x42800000, v32
	v_mul_f32_e32 v15, 0x42800000, v33
	v_cvt_pk_fp8_f32 v31, v4, v15
	s_waitcnt lgkmcnt(0)
	v_mul_f32_e32 v4, 0x42800000, v16
	v_mul_f32_e32 v15, 0x42800000, v17
	ds_read2_b32 v[16:17], v145 offset0:64 offset1:96
	ds_read2_b32 v[32:33], v145 offset1:32
	v_cvt_pk_fp8_f32 v31, v4, v15 op_sel:[0,0,1]
	v_lshl_add_u64 v[10:11], v[10:11], 0, v[6:7]
	v_add_u32_e32 v156, 0x400, v18
	s_waitcnt lgkmcnt(1)
	v_mul_f32_e32 v29, 0x42800000, v16
	v_mul_f32_e32 v36, 0x42800000, v17
	ds_read2_b32 v[16:17], v145 offset0:192 offset1:224
	s_waitcnt lgkmcnt(1)
	v_mul_f32_e32 v4, 0x42800000, v32
	v_mul_f32_e32 v15, 0x42800000, v33
	v_mov_b32_e32 v32, 0
	v_cvt_pk_fp8_f32 v32, v4, v15
	v_mul_f32_e32 v4, 0x42800000, v34
	v_mul_f32_e32 v15, 0x42800000, v35
	v_mov_b32_e32 v33, 0
	ds_read2_b32 v[34:35], v9 offset1:32
	v_cvt_pk_fp8_f32 v33, v4, v15
	s_waitcnt lgkmcnt(1)
	v_mul_f32_e32 v4, 0x42800000, v16
	v_mul_f32_e32 v15, 0x42800000, v17
	ds_read2_b32 v[16:17], v9 offset0:64 offset1:96
	v_cvt_pk_fp8_f32 v32, v29, v36 op_sel:[0,0,1]
	ds_read2_b32 v[36:37], v9 offset0:128 offset1:160
	v_cvt_pk_fp8_f32 v33, v4, v15 op_sel:[0,0,1]
	s_waitcnt lgkmcnt(2)
	v_mul_f32_e32 v4, 0x42800000, v34
	v_mul_f32_e32 v15, 0x42800000, v35
	v_mov_b32_e32 v34, 0
	v_cvt_pk_fp8_f32 v34, v4, v15
	s_waitcnt lgkmcnt(1)
	v_mul_f32_e32 v4, 0x42800000, v16
	v_mul_f32_e32 v15, 0x42800000, v17
	ds_read2_b32 v[16:17], v9 offset0:192 offset1:224
	s_waitcnt lgkmcnt(1)
	v_mul_f32_e32 v29, 0x42800000, v36
	v_mul_f32_e32 v36, 0x42800000, v37
	v_mov_b32_e32 v35, 0
	v_cvt_pk_fp8_f32 v35, v29, v36
	ds_read2_b32 v[36:37], v150 offset1:32
	v_cvt_pk_fp8_f32 v34, v4, v15 op_sel:[0,0,1]
	s_waitcnt lgkmcnt(1)
	v_mul_f32_e32 v4, 0x42800000, v16
	v_mul_f32_e32 v15, 0x42800000, v17
	ds_read2_b32 v[16:17], v150 offset0:64 offset1:96
	v_cvt_pk_fp8_f32 v35, v4, v15 op_sel:[0,0,1]
	s_waitcnt lgkmcnt(1)
	v_mul_f32_e32 v4, 0x42800000, v36
	v_mul_f32_e32 v15, 0x42800000, v37
	v_mov_b32_e32 v36, 0
	v_cvt_pk_fp8_f32 v36, v4, v15
	s_waitcnt lgkmcnt(0)
	v_mul_f32_e32 v4, 0x42800000, v16
	v_mul_f32_e32 v15, 0x42800000, v17
	ds_read2_b32 v[16:17], v150 offset0:192 offset1:224
	v_cvt_pk_fp8_f32 v36, v4, v15 op_sel:[0,0,1]
	v_mul_f32_e32 v4, 0x42800000, v38
	v_mul_f32_e32 v15, 0x42800000, v39
	v_mov_b32_e32 v37, 0
	v_cvt_pk_fp8_f32 v37, v4, v15
	s_waitcnt lgkmcnt(0)
; __device__ __forceinline__ MoeItem moe_item(const float* wg, const float* wu, const float* wd, const float* win, const float* wout, const float* wpn, const float* wpd, unsigned char* ws, int r, int lane) {
;     ...
;     const int mat = r / MOE_IE, q = r % MOE_IE, e = mat / 3, which = mat % 3, kb = q / 64, nb = q % 64, n0 = nb * 32;
;     const float* src = (which == 0 ? wg : (which == 1 ? wu : wd)) + (size_t)e * DM * DFF + (size_t)(kb * 128 + (lane >> 5)) * DFF + n0 + (lane & 31);
;     unsigned char* dst;
;     if (which < 2) dst = ws + WS_WGUT + ((size_t)(e * 16 + (n0 >> 7)) * 256 + which * 128 + (n0 & 127)) * DM;
;     else dst = ws + WS_WDT + ((size_t)e * DM + n0) * DFF;
;     MoeItem it; it.stride = DFF; it.dpitch = DM; it.src = src; it.dst = dst + kb * 128 + (size_t)(lane >> 3) * DM + 16 * (lane & 7); return it;
	v_mul_f32_e32 v4, 0x42800000, v16
	v_mul_f32_e32 v15, 0x42800000, v17
	ds_read2_b32 v[16:17], v18 offset1:32
	v_cvt_pk_fp8_f32 v37, v4, v15 op_sel:[0,0,1]
	global_store_dwordx4 v[10:11], v[30:33], off
	ds_read2_b32 v[32:33], v18 offset0:64 offset1:96
	s_lshl_b64 s[38:39], s[38:39], 3
	s_waitcnt lgkmcnt(1)
	v_mul_f32_e32 v4, 0x42800000, v16
	v_mul_f32_e32 v15, 0x42800000, v17
	ds_read2_b32 v[16:17], v18 offset0:128 offset1:160
	v_mov_b32_e32 v30, 0
	v_cvt_pk_fp8_f32 v30, v4, v15
	s_waitcnt lgkmcnt(1)
	v_mul_f32_e32 v4, 0x42800000, v32
	v_mov_b32_e32 v31, 0
	s_waitcnt lgkmcnt(0)
	v_mul_f32_e32 v29, 0x42800000, v16
	v_mul_f32_e32 v32, 0x42800000, v17
	ds_read2_b32 v[16:17], v18 offset0:192 offset1:224
	v_mul_f32_e32 v15, 0x42800000, v33
	v_cvt_pk_fp8_f32 v31, v29, v32
	ds_read2_b32 v[32:33], v156 offset1:32
	v_cvt_pk_fp8_f32 v30, v4, v15 op_sel:[0,0,1]
	s_waitcnt lgkmcnt(1)
	v_mul_f32_e32 v4, 0x42800000, v16
	v_mul_f32_e32 v15, 0x42800000, v17
	ds_read2_b32 v[16:17], v156 offset0:64 offset1:96
	v_lshl_add_u64 v[10:11], v[10:11], 0, s[38:39]
	global_store_dwordx4 v[10:11], v[34:37], off
	ds_read2_b32 v[34:35], v156 offset0:128 offset1:160
	v_cvt_pk_fp8_f32 v31, v4, v15 op_sel:[0,0,1]
	s_waitcnt lgkmcnt(2)
	v_mul_f32_e32 v4, 0x42800000, v32
	v_mul_f32_e32 v15, 0x42800000, v33
	v_mov_b32_e32 v32, 0
	v_cvt_pk_fp8_f32 v32, v4, v15
	s_waitcnt lgkmcnt(1)
	v_mul_f32_e32 v4, 0x42800000, v16
	v_mul_f32_e32 v15, 0x42800000, v17
	ds_read2_b32 v[16:17], v156 offset0:192 offset1:224
	s_waitcnt lgkmcnt(1)
	v_mul_f32_e32 v29, 0x42800000, v34
	v_mul_f32_e32 v34, 0x42800000, v35
	v_mov_b32_e32 v33, 0
	v_cvt_pk_fp8_f32 v33, v29, v34
	ds_read2_b32 v[34:35], v19 offset1:32
	v_cvt_pk_fp8_f32 v32, v4, v15 op_sel:[0,0,1]
	s_waitcnt lgkmcnt(1)
	v_mul_f32_e32 v4, 0x42800000, v16
	v_mul_f32_e32 v15, 0x42800000, v17
	ds_read2_b32 v[16:17], v19 offset0:64 offset1:96
	ds_read2_b32 v[36:37], v19 offset0:128 offset1:160
	v_cvt_pk_fp8_f32 v33, v4, v15 op_sel:[0,0,1]
	s_waitcnt lgkmcnt(2)
	v_mul_f32_e32 v4, 0x42800000, v34
	v_mul_f32_e32 v15, 0x42800000, v35
	v_mov_b32_e32 v34, 0
	v_cvt_pk_fp8_f32 v34, v4, v15
	s_waitcnt lgkmcnt(1)
	v_mul_f32_e32 v4, 0x42800000, v16
	v_mul_f32_e32 v15, 0x42800000, v17
	ds_read2_b32 v[16:17], v19 offset0:192 offset1:224
	s_waitcnt lgkmcnt(1)
	v_mul_f32_e32 v29, 0x42800000, v36
	v_mul_f32_e32 v36, 0x42800000, v37
	v_mov_b32_e32 v35, 0
	v_add_u32_e32 v160, 0x400, v19
	v_cvt_pk_fp8_f32 v35, v29, v36
	ds_read2_b32 v[36:37], v160 offset1:32
	v_cvt_pk_fp8_f32 v34, v4, v15 op_sel:[0,0,1]
	s_waitcnt lgkmcnt(1)
	v_mul_f32_e32 v4, 0x42800000, v16
	v_mul_f32_e32 v15, 0x42800000, v17
	ds_read2_b32 v[16:17], v160 offset0:64 offset1:96
	ds_read2_b32 v[38:39], v160 offset0:128 offset1:160
	v_cvt_pk_fp8_f32 v35, v4, v15 op_sel:[0,0,1]
	s_waitcnt lgkmcnt(2)
	v_mul_f32_e32 v4, 0x42800000, v36
	v_mul_f32_e32 v15, 0x42800000, v37
	v_mov_b32_e32 v36, 0
	v_cvt_pk_fp8_f32 v36, v4, v15
	s_waitcnt lgkmcnt(1)
	v_mul_f32_e32 v4, 0x42800000, v16
	v_mul_f32_e32 v15, 0x42800000, v17
	ds_read2_b32 v[16:17], v160 offset0:192 offset1:224
	s_waitcnt lgkmcnt(1)
	v_mul_f32_e32 v29, 0x42800000, v38
	v_mul_f32_e32 v38, 0x42800000, v39
	v_mov_b32_e32 v37, 0
	v_cvt_pk_fp8_f32 v37, v29, v38
	v_cvt_pk_fp8_f32 v36, v4, v15 op_sel:[0,0,1]
	s_waitcnt lgkmcnt(0)
	v_mul_f32_e32 v4, 0x42800000, v16
	v_mul_f32_e32 v15, 0x42800000, v17
	v_cvt_pk_fp8_f32 v37, v4, v15 op_sel:[0,0,1]
	v_lshl_add_u64 v[10:11], v[10:11], 0, s[38:39]
	global_store_dwordx4 v[10:11], v[30:33], off
	v_lshl_add_u64 v[10:11], v[10:11], 0, s[38:39]
	global_store_dwordx4 v[10:11], v[34:37], off
	s_waitcnt lgkmcnt(0)
	s_add_i32 s3, s89, s3
	s_min_i32 s43, s3, s7
	s_cmp_lt_i32 s43, 0x19000
	s_mov_b64 s[38:39], -1
	s_cbranch_scc0 .LBB0_126
	s_cmp_lt_i32 s43, 0x18c00
	s_cbranch_scc0 .LBB0_123
	s_cmp_lt_i32 s43, 0x18000
	s_cbranch_scc0 .LBB0_113
	s_and_b32 s4, s43, 15
	s_lshl_b32 s4, s4, 6
	s_bfe_u32 s46, s43, 0x60004
	s_and_b32 s43, s43, 0xfffffc00
	s_or_b32 s43, s43, s4
	s_or_b32 s43, s43, s46
	s_ashr_i32 s4, s43, 31
	s_lshr_b32 s4, s4, 22
	s_add_i32 s4, s43, s4
	s_ashr_i32 s39, s4, 10
	s_and_b32 s4, s4, 0xfc00
	s_sub_i32 s46, s43, s4
	s_mul_hi_i32 s4, s43, 0x2aaaaaab
	s_lshr_b32 s38, s4, 31
	s_ashr_i32 s4, s4, 9
	s_add_i32 s38, s4, s38
	s_mul_hi_i32 s4, s39, 0x55555556
	s_lshr_b32 s45, s4, 31
	s_add_i32 s4, s4, s45
	s_mul_i32 s4, s4, 3
	s_sub_i32 s4, s39, s4
	s_sext_i32_i16 s39, s46
	s_bfe_u32 s39, s39, 0x60019
	s_add_i32 s45, s46, s39
	s_and_b32 s39, s45, 0xffc0
	s_sub_i32 s39, s46, s39
	s_sext_i32_i16 s84, s39
	s_lshl_b32 s46, s84, 5
	s_ashr_i32 s39, s38, 31
	s_ashr_i32 s47, s46, 31
	s_cmp_gt_i32 s4, 1
	s_mov_b64 s[70:71], -1
	s_cbranch_scc0 .LBB0_110
	s_lshl_b64 s[68:69], s[38:39], 22
	s_lshl_b64 s[70:71], s[46:47], 11
	s_add_u32 s68, s73, s68
	s_addc_u32 s69, s74, s69
	s_add_u32 s68, s68, s70
	s_addc_u32 s69, s69, s71
	s_mov_b64 s[70:71], 0

; __global__ void __launch_bounds__(512, 2) fwd(Args args) {
	.amdhsa_kernel _Z3fwd4Args
		.amdhsa_group_segment_fixed_size 0
		.amdhsa_private_segment_fixed_size 0
		.amdhsa_kernarg_size 504
		.amdhsa_user_sgpr_count 2
		.amdhsa_user_sgpr_dispatch_ptr 0
		.amdhsa_user_sgpr_queue_ptr 0
		.amdhsa_user_sgpr_kernarg_segment_ptr 1
		.amdhsa_user_sgpr_dispatch_id 0
		.amdhsa_user_sgpr_kernarg_preload_length 0
		.amdhsa_user_sgpr_kernarg_preload_offset 0
		.amdhsa_user_sgpr_private_segment_size 0
		.amdhsa_uses_dynamic_stack 0
		.amdhsa_enable_private_segment 0
		.amdhsa_system_sgpr_workgroup_id_x 1
		.amdhsa_system_sgpr_workgroup_id_y 0
		.amdhsa_system_sgpr_workgroup_id_z 0
		.amdhsa_system_sgpr_workgroup_info 0
		.amdhsa_system_vgpr_workitem_id 0
		.amdhsa_next_free_vgpr 256
		.amdhsa_next_free_sgpr 100
		.amdhsa_accum_offset 256
		.amdhsa_reserve_vcc 1
		.amdhsa_float_round_mode_32 0
		.amdhsa_float_round_mode_16_64 0
		.amdhsa_float_denorm_mode_32 3
		.amdhsa_float_denorm_mode_16_64 3
		.amdhsa_dx10_clamp 1
		.amdhsa_ieee_mode 1
		.amdhsa_fp16_overflow 0
		.amdhsa_tg_split 0
		.amdhsa_exception_fp_ieee_invalid_op 0
		.amdhsa_exception_fp_denorm_src 0
		.amdhsa_exception_fp_ieee_div_zero 0
		.amdhsa_exception_fp_ieee_overflow 0
		.amdhsa_exception_fp_ieee_underflow 0
		.amdhsa_exception_fp_ieee_inexact 0
		.amdhsa_exception_int_div_zero 0
	.end_amdhsa_kernel

; __global__ void __launch_bounds__(512, 2) fwd(Args args) {
amdhsa.kernels:
  - .agpr_count:     0
    .args:
      - .offset:         0
        .size:           248
        .value_kind:     by_value
      - .offset:         248
        .size:           4
        .value_kind:     hidden_block_count_x
      - .offset:         252
        .size:           4
        .value_kind:     hidden_block_count_y
      - .offset:         256
        .size:           4
        .value_kind:     hidden_block_count_z
      - .offset:         260
        .size:           2
        .value_kind:     hidden_group_size_x
      - .offset:         262
        .size:           2
        .value_kind:     hidden_group_size_y
      - .offset:         264
        .size:           2
        .value_kind:     hidden_group_size_z
      - .offset:         266
        .size:           2
        .value_kind:     hidden_remainder_x
      - .offset:         268
        .size:           2
        .value_kind:     hidden_remainder_y
      - .offset:         270
        .size:           2
        .value_kind:     hidden_remainder_z
      - .offset:         288
        .size:           8
        .value_kind:     hidden_global_offset_x
      - .offset:         296
        .size:           8
        .value_kind:     hidden_global_offset_y
      - .offset:         304
        .size:           8
        .value_kind:     hidden_global_offset_z
      - .offset:         312
        .size:           2
        .value_kind:     hidden_grid_dims
      - .offset:         368
        .size:           4
        .value_kind:     hidden_dynamic_lds_size
    .group_segment_fixed_size: 0
    .kernarg_segment_align: 8
    .kernarg_segment_size: 504
    .language:       OpenCL C
    .language_version:
      - 2
      - 0
    .max_flat_workgroup_size: 512
    .name:           _Z3fwd4Args
    .private_segment_fixed_size: 0
    .sgpr_count:     106
    .sgpr_spill_count: 12
    .symbol:         _Z3fwd4Args.kd
    .uniform_work_group_size: 1
    .uses_dynamic_stack: false
    .vgpr_count:     256
    .vgpr_spill_count: 0
    .wavefront_size: 64
